# v30: v29 + router bias added in the 256-thread stage (bias kept in a VGPR for the phase), routing reads sigmoid+bias from LDS; its bias VMEM loads and vmcnt waits (behind the in-flight prefetch) remov
# baseline (speedup 1.0000x reference)
.LBB0_1729:
	s_or_b64 exec, exec, s[6:7]
	v_cmp_gt_i32_e64 s[4:5], 16, v167
	v_lshl_add_u32 v188, v167, 2, 0
	s_and_saveexec_b64 s[6:7], s[4:5]
	v_add_u32_e32 v0, 0x20400, v188
	v_mov_b32_e32 v1, 0
	ds_write_b32 v0, v1
	s_or_b64 exec, exec, s[6:7]
	v_readlane_b32 s0, v252, 3
	v_readlane_b32 s1, v252, 4
	s_load_dwordx2 s[0:1], s[0:1], 0xb8
	v_and_b32_e32 v64, 15, v161
	v_ashrrev_i32_e32 v65, 4, v161
	v_lshlrev_b32_e32 v0, 13, v64
	v_lshlrev_b32_e32 v1, 5, v65
	s_waitcnt lgkmcnt(0)
	s_add_u32 s2, s0, s2
	v_readlane_b32 s0, v252, 10
	s_addc_u32 s3, s1, s3
	s_lshl_b32 s0, s0, 10
	s_add_i32 s0, s0, 0
	v_add3_u32 v66, s0, v0, v1
	s_barrier
	ds_read_b128 v[4:7], v66
	ds_read_b128 v[8:11], v66 offset:16
	s_waitcnt lgkmcnt(1)
	v_cvt_pk_bf16_f32 v0, v4, v5
	s_nop 0
	v_lshlrev_b32_e32 v1, 16, v0
	v_and_b32_e32 v2, 0xffff0000, v0
	v_sub_f32_e32 v1, v4, v1
	v_sub_f32_e32 v2, v5, v2
	v_cvt_pk_bf16_f32 v4, v1, v2
	v_cvt_pk_bf16_f32 v1, v6, v7
	s_lshl_b32 s1, s92, 3
	v_lshlrev_b32_e32 v2, 16, v1
	v_and_b32_e32 v3, 0xffff0000, v1
	v_sub_f32_e32 v2, v6, v2
	v_sub_f32_e32 v3, v7, v3
	v_cvt_pk_bf16_f32 v5, v2, v3
	s_waitcnt lgkmcnt(0)
	v_cvt_pk_bf16_f32 v2, v8, v9
	s_lshl_b32 s33, s76, 3
	v_lshlrev_b32_e32 v3, 16, v2
	v_and_b32_e32 v6, 0xffff0000, v2
	v_sub_f32_e32 v3, v8, v3
	v_sub_f32_e32 v6, v9, v6
	v_cvt_pk_bf16_f32 v6, v3, v6
	v_cvt_pk_bf16_f32 v3, v10, v11
	s_mov_b32 s34, 0
	v_lshlrev_b32_e32 v7, 16, v3
	v_sub_f32_e32 v7, v10, v7
	v_and_b32_e32 v8, 0xffff0000, v3
	v_sub_f32_e32 v8, v11, v8
	v_cvt_pk_bf16_f32 v7, v7, v8
	ds_read_b128 v[12:15], v66 offset:128
	ds_read_b128 v[16:19], v66 offset:144
	s_waitcnt lgkmcnt(1)
	v_cvt_pk_bf16_f32 v8, v12, v13
	s_nop 0
	v_lshlrev_b32_e32 v9, 16, v8
	v_and_b32_e32 v10, 0xffff0000, v8
	v_sub_f32_e32 v9, v12, v9
	v_sub_f32_e32 v10, v13, v10
	v_cvt_pk_bf16_f32 v12, v9, v10
	v_cvt_pk_bf16_f32 v9, v14, v15
	v_mov_b32_e32 v189, v161
	v_lshlrev_b32_e32 v10, 16, v9
	v_and_b32_e32 v11, 0xffff0000, v9
	v_sub_f32_e32 v10, v14, v10
	v_sub_f32_e32 v11, v15, v11
	v_cvt_pk_bf16_f32 v13, v10, v11
	s_waitcnt lgkmcnt(0)
	v_cvt_pk_bf16_f32 v10, v16, v17
	s_cmp_lt_i32 s39, 1
	v_lshlrev_b32_e32 v11, 16, v10
	v_and_b32_e32 v14, 0xffff0000, v10
	v_sub_f32_e32 v11, v16, v11
	v_sub_f32_e32 v14, v17, v14
	v_cvt_pk_bf16_f32 v14, v11, v14
	v_cvt_pk_bf16_f32 v11, v18, v19
	s_nop 0
	v_lshlrev_b32_e32 v15, 16, v11
	v_sub_f32_e32 v15, v18, v15
	v_and_b32_e32 v16, 0xffff0000, v11
	v_sub_f32_e32 v16, v19, v16
	v_cvt_pk_bf16_f32 v15, v15, v16
	ds_read_b128 v[20:23], v66 offset:256
	ds_read_b128 v[24:27], v66 offset:272
	s_waitcnt lgkmcnt(1)
	v_cvt_pk_bf16_f32 v16, v20, v21
	s_nop 0
	v_lshlrev_b32_e32 v17, 16, v16
	v_and_b32_e32 v18, 0xffff0000, v16
	v_sub_f32_e32 v17, v20, v17
	v_sub_f32_e32 v18, v21, v18
	v_cvt_pk_bf16_f32 v20, v17, v18
	v_cvt_pk_bf16_f32 v17, v22, v23
	s_nop 0
	v_lshlrev_b32_e32 v18, 16, v17
	v_and_b32_e32 v19, 0xffff0000, v17
	v_sub_f32_e32 v18, v22, v18
	v_sub_f32_e32 v19, v23, v19
	v_cvt_pk_bf16_f32 v21, v18, v19
	s_waitcnt lgkmcnt(0)
	v_cvt_pk_bf16_f32 v18, v24, v25
	s_nop 0
	v_lshlrev_b32_e32 v19, 16, v18
	v_and_b32_e32 v22, 0xffff0000, v18
	v_sub_f32_e32 v19, v24, v19
	v_sub_f32_e32 v22, v25, v22
	v_cvt_pk_bf16_f32 v22, v19, v22
	v_cvt_pk_bf16_f32 v19, v26, v27
	s_nop 0
	v_lshlrev_b32_e32 v23, 16, v19
	v_sub_f32_e32 v23, v26, v23
	v_and_b32_e32 v24, 0xffff0000, v19
	v_sub_f32_e32 v24, v27, v24
	v_cvt_pk_bf16_f32 v23, v23, v24
	ds_read_b128 v[28:31], v66 offset:384
	ds_read_b128 v[32:35], v66 offset:400
	s_waitcnt lgkmcnt(1)
	v_cvt_pk_bf16_f32 v24, v28, v29
	s_nop 0
	v_lshlrev_b32_e32 v25, 16, v24
	v_and_b32_e32 v26, 0xffff0000, v24
	v_sub_f32_e32 v25, v28, v25
	v_sub_f32_e32 v26, v29, v26
	v_cvt_pk_bf16_f32 v28, v25, v26
	v_cvt_pk_bf16_f32 v25, v30, v31
	s_nop 0
	v_lshlrev_b32_e32 v26, 16, v25
	v_and_b32_e32 v27, 0xffff0000, v25
	v_sub_f32_e32 v26, v30, v26
	v_sub_f32_e32 v27, v31, v27
	v_cvt_pk_bf16_f32 v29, v26, v27
	s_waitcnt lgkmcnt(0)
	v_cvt_pk_bf16_f32 v26, v32, v33
	s_nop 0
	v_lshlrev_b32_e32 v27, 16, v26
	v_and_b32_e32 v30, 0xffff0000, v26
	v_sub_f32_e32 v27, v32, v27
	v_sub_f32_e32 v30, v33, v30
	v_cvt_pk_bf16_f32 v30, v27, v30
	v_cvt_pk_bf16_f32 v27, v34, v35
	s_nop 0
	v_lshlrev_b32_e32 v31, 16, v27
	v_sub_f32_e32 v31, v34, v31
	v_and_b32_e32 v32, 0xffff0000, v27
	v_sub_f32_e32 v32, v35, v32
	v_cvt_pk_bf16_f32 v31, v31, v32
	s_waitcnt vmcnt(7)
	ds_read_b128 v[36:39], v66 offset:512
	ds_read_b128 v[40:43], v66 offset:528
	s_waitcnt lgkmcnt(1)
	v_cvt_pk_bf16_f32 v32, v36, v37
	s_nop 0
	v_lshlrev_b32_e32 v33, 16, v32
	v_and_b32_e32 v34, 0xffff0000, v32
	v_sub_f32_e32 v33, v36, v33
	v_sub_f32_e32 v34, v37, v34
	v_cvt_pk_bf16_f32 v36, v33, v34
	v_cvt_pk_bf16_f32 v33, v38, v39
	s_nop 0
	v_lshlrev_b32_e32 v34, 16, v33
	v_and_b32_e32 v35, 0xffff0000, v33
	v_sub_f32_e32 v34, v38, v34
	v_sub_f32_e32 v35, v39, v35
	v_cvt_pk_bf16_f32 v37, v34, v35
	s_waitcnt lgkmcnt(0)
	v_cvt_pk_bf16_f32 v34, v40, v41
	s_nop 0
	v_lshlrev_b32_e32 v35, 16, v34
	v_and_b32_e32 v38, 0xffff0000, v34
	v_sub_f32_e32 v35, v40, v35
	v_sub_f32_e32 v38, v41, v38
	v_cvt_pk_bf16_f32 v38, v35, v38
	v_cvt_pk_bf16_f32 v35, v42, v43
	s_nop 0
	v_lshlrev_b32_e32 v39, 16, v35
	v_sub_f32_e32 v39, v42, v39
	v_and_b32_e32 v40, 0xffff0000, v35
	v_sub_f32_e32 v40, v43, v40
	v_cvt_pk_bf16_f32 v39, v39, v40
	s_waitcnt vmcnt(1)
	ds_read_b128 v[44:47], v66 offset:640
	s_waitcnt vmcnt(0)
	ds_read_b128 v[48:51], v66 offset:656
	s_waitcnt lgkmcnt(1)
	v_cvt_pk_bf16_f32 v40, v44, v45
	s_nop 0
	v_lshlrev_b32_e32 v41, 16, v40
	v_and_b32_e32 v42, 0xffff0000, v40
	v_sub_f32_e32 v41, v44, v41
	v_sub_f32_e32 v42, v45, v42
	v_cvt_pk_bf16_f32 v44, v41, v42
	v_cvt_pk_bf16_f32 v41, v46, v47
	s_nop 0
	v_lshlrev_b32_e32 v42, 16, v41
	v_and_b32_e32 v43, 0xffff0000, v41
	v_sub_f32_e32 v42, v46, v42
	v_sub_f32_e32 v43, v47, v43
	v_cvt_pk_bf16_f32 v45, v42, v43
	s_waitcnt lgkmcnt(0)
	v_cvt_pk_bf16_f32 v42, v48, v49
	s_nop 0
	v_lshlrev_b32_e32 v43, 16, v42
	v_and_b32_e32 v46, 0xffff0000, v42
	v_sub_f32_e32 v43, v48, v43
	v_sub_f32_e32 v46, v49, v46
	v_cvt_pk_bf16_f32 v46, v43, v46
	v_cvt_pk_bf16_f32 v43, v50, v51
	s_nop 0
	v_lshlrev_b32_e32 v47, 16, v43
	v_sub_f32_e32 v47, v50, v47
	v_and_b32_e32 v48, 0xffff0000, v43
	v_sub_f32_e32 v48, v51, v48
	v_cvt_pk_bf16_f32 v47, v47, v48
	ds_read_b128 v[52:55], v66 offset:768
	ds_read_b128 v[56:59], v66 offset:784
	s_waitcnt lgkmcnt(1)
	v_cvt_pk_bf16_f32 v48, v52, v53
	s_nop 0
	v_lshlrev_b32_e32 v49, 16, v48
	v_and_b32_e32 v50, 0xffff0000, v48
	v_sub_f32_e32 v49, v52, v49
	v_sub_f32_e32 v50, v53, v50
	v_cvt_pk_bf16_f32 v52, v49, v50
	v_cvt_pk_bf16_f32 v49, v54, v55
	s_nop 0
	v_lshlrev_b32_e32 v50, 16, v49
	v_and_b32_e32 v51, 0xffff0000, v49
	v_sub_f32_e32 v50, v54, v50
	v_sub_f32_e32 v51, v55, v51
	v_cvt_pk_bf16_f32 v53, v50, v51
	s_waitcnt lgkmcnt(0)
	v_cvt_pk_bf16_f32 v50, v56, v57
	s_nop 0
	v_lshlrev_b32_e32 v51, 16, v50
	v_and_b32_e32 v54, 0xffff0000, v50
	v_sub_f32_e32 v51, v56, v51
	v_sub_f32_e32 v54, v57, v54
	v_cvt_pk_bf16_f32 v54, v51, v54
	v_cvt_pk_bf16_f32 v51, v58, v59
	s_nop 0
	v_lshlrev_b32_e32 v55, 16, v51
	v_sub_f32_e32 v55, v58, v55
	v_and_b32_e32 v56, 0xffff0000, v51
	v_sub_f32_e32 v56, v59, v56
	v_cvt_pk_bf16_f32 v55, v55, v56
	ds_read_b128 v[60:63], v66 offset:896
	ds_read_b128 v[66:69], v66 offset:912
	s_waitcnt lgkmcnt(1)
	v_cvt_pk_bf16_f32 v56, v60, v61
	s_nop 0
	v_lshlrev_b32_e32 v57, 16, v56
	v_and_b32_e32 v58, 0xffff0000, v56
	v_sub_f32_e32 v57, v60, v57
	v_sub_f32_e32 v58, v61, v58
	v_cvt_pk_bf16_f32 v60, v57, v58
	v_cvt_pk_bf16_f32 v57, v62, v63
	s_nop 0
	v_lshlrev_b32_e32 v58, 16, v57
	v_and_b32_e32 v59, 0xffff0000, v57
	v_sub_f32_e32 v58, v62, v58
	v_sub_f32_e32 v59, v63, v59
	v_cvt_pk_bf16_f32 v61, v58, v59
	s_waitcnt lgkmcnt(0)
	v_cvt_pk_bf16_f32 v58, v66, v67
	s_nop 0
	v_lshlrev_b32_e32 v59, 16, v58
	v_and_b32_e32 v62, 0xffff0000, v58
	v_sub_f32_e32 v59, v66, v59
	v_sub_f32_e32 v62, v67, v62
	v_cvt_pk_bf16_f32 v62, v59, v62
	v_cvt_pk_bf16_f32 v59, v68, v69
	s_nop 0
	v_lshlrev_b32_e32 v63, 16, v59
	v_sub_f32_e32 v63, v68, v63
	v_and_b32_e32 v66, 0xffff0000, v59
	v_sub_f32_e32 v66, v69, v66
	v_cvt_pk_bf16_f32 v63, v63, v66
	s_barrier
	s_cbranch_scc1 .LBB0_1858
	s_add_u32 s35, s2, 0x1c9c8000
	s_addc_u32 s36, s3, 0
	s_add_u32 s37, s2, 0x149c8000
	v_readlane_b32 s10, v252, 10
	s_addc_u32 s40, s3, 0
	s_add_i32 s18, s10, s33
	s_add_u32 s41, s2, 0x249c8000
	s_addc_u32 s42, s3, 0
	s_add_i32 s6, s18, s1
	s_ashr_i32 s7, s6, 31
	s_lshl_b64 s[8:9], s[6:7], 11
	s_add_u32 s8, s37, s8
	s_addc_u32 s9, s40, s9
	v_lshlrev_b32_e32 v66, 2, v189
	s_lshl_b64 s[6:7], s[6:7], 12
	v_ashrrev_i32_e32 v67, 31, v66
	s_add_u32 s6, s35, s6
	s_addc_u32 s7, s36, s7
	v_lshlrev_b64 v[70:71], 1, v[66:67]
	s_ashr_i32 s19, s18, 31
	v_lshl_add_u64 v[72:73], s[6:7], 0, v[70:71]
	s_lshl_b64 s[6:7], s[18:19], 11
	s_add_u32 s6, s37, s6
	s_addc_u32 s7, s40, s7
	v_lshl_add_u64 v[68:69], s[8:9], 0, v[66:67]
	v_lshl_add_u64 v[66:67], s[6:7], 0, v[66:67]
	s_lshl_b64 s[6:7], s[18:19], 12
	s_add_u32 s6, s35, s6
	s_addc_u32 s7, s36, s7
	global_load_dwordx2 v[136:137], v[72:73], off offset:3584
	global_load_dwordx2 v[132:133], v[72:73], off offset:3072
	global_load_dwordx2 v[90:91], v[72:73], off offset:2560
	global_load_dwordx2 v[88:89], v[72:73], off offset:2048
	global_load_dword v154, v[68:69], off offset:1792
	global_load_dword v155, v[68:69], off offset:1536
	global_load_dword v160, v[68:69], off offset:1280
	global_load_dword v166, v[68:69], off offset:1024
	global_load_dword v168, v[68:69], off offset:768
	global_load_dword v169, v[68:69], off offset:512
	global_load_dword v172, v[68:69], off offset:256
	global_load_dword v170, v[68:69], off
	global_load_dwordx2 v[138:139], v[72:73], off offset:1536
	global_load_dwordx2 v[128:129], v[72:73], off offset:1024
	global_load_dwordx2 v[140:141], v[72:73], off offset:512
	global_load_dwordx2 v[142:143], v[72:73], off
	v_lshl_add_u64 v[68:69], s[6:7], 0, v[70:71]
	global_load_dwordx2 v[144:145], v[68:69], off offset:3584
	global_load_dwordx2 v[86:87], v[68:69], off offset:3072
	global_load_dwordx2 v[82:83], v[68:69], off offset:2560
	global_load_dwordx2 v[80:81], v[68:69], off offset:2048
	global_load_dword v171, v[66:67], off offset:1792
	global_load_dword v173, v[66:67], off offset:1536
	global_load_dword v134, v[66:67], off offset:1280
	global_load_dword v135, v[66:67], off offset:1024
	global_load_dword v148, v[66:67], off offset:768
	global_load_dword v149, v[66:67], off offset:512
	global_load_dword v150, v[66:67], off offset:256
	global_load_dword v146, v[66:67], off
	global_load_dwordx2 v[92:93], v[68:69], off offset:1536
	global_load_dwordx2 v[84:85], v[68:69], off offset:1024
	global_load_dwordx2 v[94:95], v[68:69], off offset:512
	global_load_dwordx2 v[130:131], v[68:69], off
	v_lshl_add_u32 v65, s10, 5, v65
	v_lshl_add_u32 v66, v64, 12, 0
	v_xor_b32_e32 v69, v65, v64
	v_lshl_add_u32 v190, v69, 4, v66
	v_add_u32_e32 v69, 4, v65
	s_lshl_b32 s43, s10, 1
	s_add_i32 s6, s0, 0x22000
	v_xor_b32_e32 v69, v69, v64
	s_add_u32 s20, s2, 0x468000
	v_lshl_add_u32 v192, v69, 4, v66
	v_add_u32_e32 v69, 8, v65
	s_addc_u32 s21, s3, 0
	v_xor_b32_e32 v69, v69, v64
	s_add_u32 s22, s2, 0x488000
	v_lshl_add_u32 v194, v69, 4, v66
	v_add_u32_e32 v69, 12, v65
	v_lshl_add_u32 v67, v64, 6, s6
	s_addc_u32 s23, s3, 0
	s_lshl_b32 s6, s10, 13
	s_or_b32 s45, s43, 1
	v_xor_b32_e32 v69, v69, v64
	s_add_i32 s44, s6, 0
	s_lshl_b32 s6, s45, 12
	v_lshl_add_u32 v196, v69, 4, v66
	v_add_u32_e32 v69, 16, v65
	s_add_i32 s46, s6, 0
	v_xor_b32_e32 v69, v69, v64
	v_readlane_b32 s6, v252, 3
	v_lshl_add_u32 v198, v69, 4, v66
	v_add_u32_e32 v69, 20, v65
	v_readlane_b32 s7, v252, 4
	v_xor_b32_e32 v69, v69, v64
	s_load_dwordx2 s[24:25], s[6:7], 0x28
	s_load_dwordx2 s[26:27], s[6:7], 0x88
	v_lshl_add_u32 v200, v69, 4, v66
	v_add_u32_e32 v69, 24, v65
	v_add_u32_e32 v65, 28, v65
	v_xor_b32_e32 v69, v69, v64
	v_xor_b32_e32 v64, v65, v64
	v_and_b32_e32 v68, -16, v161
	v_lshl_add_u32 v202, v69, 4, v66
	v_lshl_add_u32 v204, v64, 4, v66
	v_add_u32_e32 v191, 0x10000, v190
	v_add_u32_e32 v193, 0x10000, v192
	v_add_u32_e32 v195, 0x10000, v194
	v_add_u32_e32 v197, 0x10000, v196
	v_add_u32_e32 v199, 0x10000, v198
	v_add_u32_e32 v201, 0x10000, v200
	v_add_u32_e32 v203, 0x10000, v202
	v_add_u32_e32 v205, 0x10000, v204
	s_mul_i32 s47, s92, 24
	s_movk_i32 s48, 0x100
	v_mov_b32_e32 v206, 0x358637bd
	s_mov_b32 s49, 0xf800000
	v_mov_b32_e32 v207, 0x260
	v_add_u32_e32 v208, v67, v68
	v_mov_b32_e32 v209, 0
	s_mov_b32 s50, 0xbfb8aa3b
	s_mov_b32 s51, 0x42ce8ed0
	s_mov_b32 s52, 0xc2b17218
	s_mov_b32 s53, 0xf149f2ca
	v_mov_b32_e32 v210, 1
	s_add_i32 s54, 0, 0x20400
	s_add_i32 s55, 0, 0x20500
	v_mov_b32_e32 v211, 0x7f800000
	s_mov_b32 s56, 0
	s_waitcnt lgkmcnt(0)
	v_and_b32_e32 v249, 15, v167
	v_lshlrev_b32_e32 v249, 2, v249
	global_load_dword v249, v249, s[26:27]
	s_branch .LBB0_1737

.Lpf_skip_0:
	v_lshlrev_b32_e32 v90, 16, v88
	v_and_b32_e32 v91, 0xffff0000, v88
	v_sub_f32_e32 v90, v86, v90
	v_sub_f32_e32 v91, v87, v91
	v_cvt_pk_bf16_f32 v89, v84, v85
	v_cvt_pk_bf16_f32 v90, v90, v91
	v_lshlrev_b32_e32 v128, 4, v128
	v_lshlrev_b32_e32 v91, 16, v89
	v_sub_f32_e32 v91, v84, v91
	v_and_b32_e32 v129, 0xffff0000, v89
	v_add3_u32 v128, s46, v128, v228
	v_sub_f32_e32 v129, v85, v129
	v_cvt_pk_bf16_f32 v91, v91, v129
	ds_write_b64 v128, v[88:89]
	v_add_u32_e32 v88, 0x10000, v128
	ds_write_b64 v88, v[90:91]
	v_mov_b32_e32 v90, 0
	v_cvt_pk_fp8_f32 v90, v154, v155
	v_mov_b32_e32 v91, 0
	v_cvt_pk_fp8_f32 v91, v174, v175
	v_lshl_add_u64 v[88:89], s[6:7], 0, v[78:79]
	v_cvt_pk_fp8_f32 v90, v152, v153 op_sel:[0,0,1]
	v_mov_b32_e32 v128, 0
	v_cvt_pk_fp8_f32 v91, v170, v171 op_sel:[0,0,1]
	v_cvt_pk_fp8_f32 v128, v186, v187
	global_store_dword v[88:89], v90, off
	v_lshl_add_u64 v[88:89], s[6:7], 0, v[76:77]
	v_mov_b32_e32 v90, 0
	global_store_dword v[88:89], v91, off
	v_cvt_pk_fp8_f32 v90, v158, v159
	v_mov_b32_e32 v91, 0
	v_cvt_pk_fp8_f32 v91, v178, v179
	v_cvt_pk_fp8_f32 v128, v184, v185 op_sel:[0,0,1]
	v_cvt_pk_fp8_f32 v90, v156, v157 op_sel:[0,0,1]
	v_lshl_add_u64 v[88:89], s[6:7], 0, v[74:75]
	v_cvt_pk_fp8_f32 v91, v176, v177 op_sel:[0,0,1]
	global_store_dword v[88:89], v128, off
	v_lshl_add_u64 v[88:89], s[6:7], 0, v[72:73]
	v_mov_b32_e32 v128, 0
	global_store_dword v[88:89], v90, off
	v_lshl_add_u64 v[88:89], s[6:7], 0, v[70:71]
	v_cvt_pk_fp8_f32 v128, v134, v135
	global_store_dword v[88:89], v91, off
	v_mov_b32_e32 v88, 0
	v_cvt_pk_fp8_f32 v88, v240, v241
	v_mov_b32_e32 v89, 0
	v_cvt_pk_fp8_f32 v89, v80, v81
	v_cvt_pk_fp8_f32 v128, v130, v131 op_sel:[0,0,1]
	v_cvt_pk_fp8_f32 v88, v238, v239 op_sel:[0,0,1]
	v_lshl_add_u64 v[80:81], s[6:7], 0, v[68:69]
	v_cvt_pk_fp8_f32 v89, v82, v83 op_sel:[0,0,1]
	global_store_dword v[80:81], v128, off
	v_lshl_add_u64 v[80:81], s[6:7], 0, v[66:67]
	global_store_dword v[80:81], v88, off
	v_lshl_add_u64 v[80:81], s[6:7], 0, v[64:65]
	global_store_dword v[80:81], v89, off
	v_mov_b32_e32 v80, 0
	v_mov_b32_e32 v81, 0
	v_cvt_pk_fp8_f32 v80, v146, v147
	v_cvt_pk_fp8_f32 v81, v164, v165
	s_add_i32 s6, s1, s18
	s_ashr_i32 s7, s6, 31
	s_lshl_b64 s[6:7], s[6:7], 11
	v_cvt_pk_fp8_f32 v80, v136, v137 op_sel:[0,0,1]
	v_cvt_pk_fp8_f32 v81, v162, v163 op_sel:[0,0,1]
	s_add_u32 s6, s41, s6
	s_addc_u32 s7, s42, s7
	v_lshl_add_u64 v[78:79], s[6:7], 0, v[78:79]
	v_lshl_add_u64 v[76:77], s[6:7], 0, v[76:77]
	v_mov_b32_e32 v82, 0
	global_store_dword v[78:79], v80, off
	global_store_dword v[76:77], v81, off
	v_mov_b32_e32 v76, 0
	v_mov_b32_e32 v77, 0
	v_cvt_pk_fp8_f32 v82, v182, v183
	v_cvt_pk_fp8_f32 v76, v150, v151
	v_cvt_pk_fp8_f32 v77, v172, v173
	v_lshl_add_u64 v[74:75], s[6:7], 0, v[74:75]
	v_cvt_pk_fp8_f32 v82, v180, v181 op_sel:[0,0,1]
	v_cvt_pk_fp8_f32 v76, v148, v149 op_sel:[0,0,1]
	v_cvt_pk_fp8_f32 v77, v168, v169 op_sel:[0,0,1]
	v_lshl_add_u64 v[72:73], s[6:7], 0, v[72:73]
	v_lshl_add_u64 v[70:71], s[6:7], 0, v[70:71]
	global_store_dword v[74:75], v82, off
	v_mov_b32_e32 v74, 0
	global_store_dword v[72:73], v76, off
	global_store_dword v[70:71], v77, off
	v_mov_b32_e32 v70, 0
	v_mov_b32_e32 v71, 0
	v_cvt_pk_fp8_f32 v74, v94, v95
	v_cvt_pk_fp8_f32 v70, v140, v141
	v_cvt_pk_fp8_f32 v71, v86, v87
	v_lshl_add_u64 v[68:69], s[6:7], 0, v[68:69]
	v_cvt_pk_fp8_f32 v74, v92, v93 op_sel:[0,0,1]
	v_cvt_pk_fp8_f32 v70, v138, v139 op_sel:[0,0,1]
	v_cvt_pk_fp8_f32 v71, v84, v85 op_sel:[0,0,1]
	v_lshl_add_u64 v[66:67], s[6:7], 0, v[66:67]
	v_lshl_add_u64 v[64:65], s[6:7], 0, v[64:65]
	global_store_dword v[68:69], v74, off
	global_store_dword v[66:67], v70, off
	global_store_dword v[64:65], v71, off
	s_waitcnt lgkmcnt(0)
	s_barrier
	ds_read_b128 v[64:67], v190
	ds_read_b128 v[68:71], v191
	s_waitcnt lgkmcnt(1)
	v_mfma_f32_16x16x32_bf16 v[72:75], v[0:3], v[64:67], 0
	v_mov_b32_e32 v128, v167
	v_mfma_f32_16x16x32_bf16 v[64:67], v[4:7], v[64:67], v[72:75]
	s_waitcnt lgkmcnt(0)
	v_mfma_f32_16x16x32_bf16 v[64:67], v[0:3], v[68:71], v[64:67]
	ds_read_b128 v[68:71], v192
	s_nop 2
	ds_read_b128 v[72:75], v193
	s_waitcnt lgkmcnt(1)
	v_mfma_f32_16x16x32_bf16 v[64:67], v[8:11], v[68:71], v[64:67]
	v_mfma_f32_16x16x32_bf16 v[64:67], v[12:15], v[68:71], v[64:67]
	s_waitcnt lgkmcnt(0)
	v_mfma_f32_16x16x32_bf16 v[64:67], v[8:11], v[72:75], v[64:67]
	ds_read_b128 v[68:71], v194
	ds_read_b128 v[72:75], v195
	s_waitcnt lgkmcnt(1)
	v_mfma_f32_16x16x32_bf16 v[64:67], v[16:19], v[68:71], v[64:67]
	v_mfma_f32_16x16x32_bf16 v[64:67], v[20:23], v[68:71], v[64:67]
	s_waitcnt lgkmcnt(0)
	v_mfma_f32_16x16x32_bf16 v[64:67], v[16:19], v[72:75], v[64:67]
	ds_read_b128 v[68:71], v196
	ds_read_b128 v[72:75], v197
	s_waitcnt lgkmcnt(1)
	v_mfma_f32_16x16x32_bf16 v[64:67], v[24:27], v[68:71], v[64:67]
	v_mfma_f32_16x16x32_bf16 v[64:67], v[28:31], v[68:71], v[64:67]
	s_waitcnt lgkmcnt(0)
	v_mfma_f32_16x16x32_bf16 v[64:67], v[24:27], v[72:75], v[64:67]
	ds_read_b128 v[68:71], v198
	ds_read_b128 v[72:75], v199
	s_waitcnt lgkmcnt(1)
	v_mfma_f32_16x16x32_bf16 v[64:67], v[32:35], v[68:71], v[64:67]
	v_mfma_f32_16x16x32_bf16 v[64:67], v[36:39], v[68:71], v[64:67]
	s_waitcnt lgkmcnt(0)
	v_mfma_f32_16x16x32_bf16 v[64:67], v[32:35], v[72:75], v[64:67]
	ds_read_b128 v[68:71], v200
	ds_read_b128 v[72:75], v201
	s_waitcnt lgkmcnt(1)
	v_mfma_f32_16x16x32_bf16 v[64:67], v[40:43], v[68:71], v[64:67]
	v_mfma_f32_16x16x32_bf16 v[64:67], v[44:47], v[68:71], v[64:67]
	s_waitcnt lgkmcnt(0)
	v_mfma_f32_16x16x32_bf16 v[64:67], v[40:43], v[72:75], v[64:67]
	ds_read_b128 v[68:71], v202
	ds_read_b128 v[72:75], v203
	s_waitcnt lgkmcnt(1)
	v_mfma_f32_16x16x32_bf16 v[64:67], v[48:51], v[68:71], v[64:67]
	v_mfma_f32_16x16x32_bf16 v[64:67], v[52:55], v[68:71], v[64:67]
	s_waitcnt lgkmcnt(0)
	v_mfma_f32_16x16x32_bf16 v[64:67], v[48:51], v[72:75], v[64:67]
	ds_read_b128 v[68:71], v204
	ds_read_b128 v[72:75], v205
	s_waitcnt lgkmcnt(1)
	v_mfma_f32_16x16x32_bf16 v[64:67], v[56:59], v[68:71], v[64:67]
	v_mfma_f32_16x16x32_bf16 v[64:67], v[60:63], v[68:71], v[64:67]
	s_waitcnt lgkmcnt(0)
	v_mfma_f32_16x16x32_bf16 v[64:67], v[56:59], v[72:75], v[64:67]
	s_nop 7
	ds_write_b128 v208, v[64:67]
	s_waitcnt lgkmcnt(0)
	s_barrier
	s_nop 0
	v_cmp_gt_i32_e32 vcc, s48, v128
	s_and_saveexec_b64 s[6:7], vcc
	s_cbranch_execz .LBB0_1743
	v_lshl_add_u32 v72, v128, 2, 0
	v_add_u32_e32 v70, 0x22000, v72
	ds_read2st64_b32 v[64:65], v70 offset1:4
	ds_read2st64_b32 v[66:67], v70 offset0:8 offset1:12
	ds_read2st64_b32 v[68:69], v70 offset0:16 offset1:20
	ds_read2st64_b32 v[70:71], v70 offset0:24 offset1:28
	s_waitcnt lgkmcnt(3)
	v_add_f32_e32 v64, 0, v64
	v_add_f32_e32 v64, v64, v65
	s_waitcnt lgkmcnt(2)
	v_add_f32_e32 v64, v64, v66
	v_add_f32_e32 v64, v64, v67
	s_waitcnt lgkmcnt(1)
	v_add_f32_e32 v64, v64, v68
	v_add_f32_e32 v64, v64, v69
	s_waitcnt lgkmcnt(0)
	v_add_f32_e32 v64, v64, v70
	v_add_f32_e32 v64, v64, v71
	v_add_u32_e32 v65, 0x21000, v72
	ds_write_b32 v65, v64
	v_mul_f32_e32 v142, 0xbfb8aa3b, v64
	v_fma_f32 v143, v64, s50, -v142
	v_rndne_f32_e32 v144, v142
	v_fmac_f32_e32 v143, 0xb2a5705f, v64
	v_sub_f32_e32 v142, v142, v144
	v_add_f32_e32 v142, v142, v143
	v_cvt_i32_f32_e32 v145, v144
	v_exp_f32_e32 v146, v142
	v_cmp_nlt_f32_e32 vcc, s51, v64
	v_ldexp_f32 v145, v146, v145
	s_nop 0
	v_cndmask_b32_e32 v145, 0, v145, vcc
	v_cmp_ngt_f32_e32 vcc, s52, v64
	s_nop 1
	v_cndmask_b32_e32 v145, v211, v145, vcc
	v_add_f32_e32 v145, 1.0, v145
	v_div_scale_f32 v146, s[98:99], v145, v145, 1.0
	v_rcp_f32_e32 v147, v146
	v_div_scale_f32 v148, vcc, 1.0, v145, 1.0
	v_fma_f32 v149, -v146, v147, 1.0
	v_fmac_f32_e32 v147, v149, v147
	v_mul_f32_e32 v149, v148, v147
	v_fma_f32 v150, -v146, v149, v148
	v_fmac_f32_e32 v149, v150, v147
	v_fma_f32 v146, -v146, v149, v148
	v_div_fmas_f32 v146, v146, v147, v149
	v_div_fixup_f32 v146, v146, v145, 1.0
	ds_write_b32 v65, v146 offset:1024
	v_add_f32_e32 v147, v249, v146
	ds_write_b32 v65, v147 offset:2048
.LBB0_1743:
	s_or_b64 exec, exec, s[6:7]
	v_cmp_gt_i32_e32 vcc, 16, v128
	s_waitcnt lgkmcnt(0)
	s_barrier
	s_and_saveexec_b64 s[28:29], vcc
	s_cbranch_execz .LBB0_1736
	v_lshl_add_u32 v68, v128, 6, 0
	v_add_u32_e32 v68, 0x21000, v68
	ds_read_b128 v[142:145], v68 offset:2048
	ds_read_b128 v[146:149], v68 offset:2064
	ds_read_b128 v[150:153], v68 offset:2080
	ds_read_b128 v[154:157], v68 offset:2096
	ds_read_b128 v[168:171], v68 offset:1024
	ds_read_b128 v[172:175], v68 offset:1040
	ds_read_b128 v[176:179], v68 offset:1056
	ds_read_b128 v[180:183], v68 offset:1072
	ds_read_b128 v[92:95], v68
	ds_read_b128 v[84:87], v68 offset:16
	s_waitcnt lgkmcnt(1)
	ds_read_b128 v[76:79], v68 offset:32
	ds_read_b128 v[68:71], v68 offset:48
	s_nop 1
	s_nop 1
	v_mov_b32_e32 v132, v168
	v_mov_b32_e32 v92, v169
	v_mov_b32_e32 v93, v142
	v_mov_b32_e32 v88, v143
	v_max_f32_e32 v89, 0xf149f2ca, v93
	v_cmp_lt_f32_e64 s[8:9], s53, v93
	v_mov_b32_e32 v129, v88
	v_cmp_ngt_f32_e64 s[6:7], v88, v89
	v_mov_b32_e32 v130, v89
	s_and_saveexec_b64 s[10:11], s[6:7]
	s_cbranch_execz .LBB0_1748
	v_mov_b32_e32 v130, 0xf149f2ca
	v_cmp_gt_f32_e32 vcc, v88, v130
	s_and_saveexec_b64 s[12:13], vcc
	v_mov_b32_e32 v130, v88
	s_or_b64 exec, exec, s[12:13]
	v_mov_b32_e32 v129, v89
.LBB0_1748:
	s_or_b64 exec, exec, s[10:11]
	s_nop 0
	s_nop 1
	s_nop 0
	v_mov_b32_e32 v93, v170
	v_mov_b32_e32 v90, v144
	v_cmp_ngt_f32_e32 vcc, v90, v129
	v_mov_b32_e32 v133, v90
	s_and_saveexec_b64 s[10:11], vcc
	s_cbranch_execz .LBB0_1752
	v_cmp_gt_f32_e32 vcc, v90, v130
	s_and_saveexec_b64 s[12:13], vcc
	v_mov_b32_e32 v130, v90
	s_or_b64 exec, exec, s[12:13]
	v_mov_b32_e32 v133, v129
	v_mov_b32_e32 v129, v130
.LBB0_1752:
	s_or_b64 exec, exec, s[10:11]
	s_nop 0
	s_nop 1
	s_nop 0
	v_mov_b32_e32 v130, v171
	v_mov_b32_e32 v131, v145
	v_cmp_ngt_f32_e32 vcc, v131, v133
	v_mov_b32_e32 v134, v131
	s_and_saveexec_b64 s[10:11], vcc
	s_cbranch_execz .LBB0_1756
	v_cmp_gt_f32_e32 vcc, v131, v129
	s_and_saveexec_b64 s[12:13], vcc
	v_mov_b32_e32 v129, v131
	s_or_b64 exec, exec, s[12:13]
	v_mov_b32_e32 v134, v133
	v_mov_b32_e32 v133, v129
.LBB0_1756:
	s_or_b64 exec, exec, s[10:11]
	s_waitcnt lgkmcnt(2)
	v_mov_b32_e32 v91, v172
	v_mov_b32_e32 v84, v146
	s_nop 0
	v_mov_b32_e32 v85, v173
	v_mov_b32_e32 v80, v147
	v_max_f32_e32 v95, 0xf149f2ca, v84
	v_cmp_ngt_f32_e32 vcc, v80, v95
	v_mov_b32_e32 v94, v80
	s_and_saveexec_b64 s[10:11], vcc
	s_cbranch_execz .LBB0_1760
	v_mov_b32_e32 v81, 0xf149f2ca
	v_cmp_gt_f32_e32 vcc, v80, v81
	s_and_saveexec_b64 s[12:13], vcc
	v_mov_b32_e32 v81, v80
	s_or_b64 exec, exec, s[12:13]
	v_mov_b32_e32 v94, v95
	v_mov_b32_e32 v95, v81
.LBB0_1760:
	s_or_b64 exec, exec, s[10:11]
	s_nop 0
	s_nop 1
	s_nop 0
	v_mov_b32_e32 v81, v174
	v_mov_b32_e32 v86, v148
	v_cmp_ngt_f32_e32 vcc, v86, v94
	v_mov_b32_e32 v135, v86
	s_and_saveexec_b64 s[10:11], vcc
	s_cbranch_execz .LBB0_1764
	v_cmp_gt_f32_e32 vcc, v86, v95
	s_and_saveexec_b64 s[12:13], vcc
	v_mov_b32_e32 v95, v86
	s_or_b64 exec, exec, s[12:13]
	v_mov_b32_e32 v135, v94
	v_mov_b32_e32 v94, v95
.LBB0_1764:
	s_or_b64 exec, exec, s[10:11]
	s_nop 0
	s_nop 1
	s_nop 0
	v_mov_b32_e32 v95, v175
	v_mov_b32_e32 v129, v149
	v_cmp_ngt_f32_e32 vcc, v129, v135
	v_mov_b32_e32 v136, v129
	s_and_saveexec_b64 s[10:11], vcc
	s_cbranch_execz .LBB0_1768
	v_cmp_gt_f32_e32 vcc, v129, v94
	s_and_saveexec_b64 s[12:13], vcc
	v_mov_b32_e32 v94, v129
	s_or_b64 exec, exec, s[12:13]
	v_mov_b32_e32 v136, v135
	v_mov_b32_e32 v135, v94
.LBB0_1768:
	s_or_b64 exec, exec, s[10:11]
	s_waitcnt lgkmcnt(1)
	v_mov_b32_e32 v83, v176
	v_mov_b32_e32 v76, v150
	s_nop 0
	v_mov_b32_e32 v77, v177
	v_mov_b32_e32 v72, v151
	v_max_f32_e32 v87, 0xf149f2ca, v76
	v_cmp_ngt_f32_e32 vcc, v72, v87
	v_mov_b32_e32 v73, v72
	s_and_saveexec_b64 s[10:11], vcc
	s_cbranch_execz .LBB0_1772
	v_mov_b32_e32 v82, 0xf149f2ca
	v_cmp_gt_f32_e32 vcc, v72, v82
	s_and_saveexec_b64 s[12:13], vcc
	v_mov_b32_e32 v82, v72
	s_or_b64 exec, exec, s[12:13]
	v_mov_b32_e32 v73, v87
	v_mov_b32_e32 v87, v82
.LBB0_1772:
	s_or_b64 exec, exec, s[10:11]
	s_nop 0
	s_nop 1
	s_nop 0
	v_mov_b32_e32 v78, v178
	v_mov_b32_e32 v82, v152
	v_cmp_ngt_f32_e32 vcc, v82, v73
	v_mov_b32_e32 v137, v82
	s_and_saveexec_b64 s[10:11], vcc
	s_cbranch_execz .LBB0_1776
	v_cmp_gt_f32_e32 vcc, v82, v87
	s_and_saveexec_b64 s[12:13], vcc
	v_mov_b32_e32 v87, v82
	s_or_b64 exec, exec, s[12:13]
	v_mov_b32_e32 v137, v73
	v_mov_b32_e32 v73, v87
.LBB0_1776:
	s_or_b64 exec, exec, s[10:11]
	s_nop 0
	s_nop 1
	s_nop 0
	v_mov_b32_e32 v87, v179
	v_mov_b32_e32 v94, v153
	v_cmp_ngt_f32_e32 vcc, v94, v137
	v_mov_b32_e32 v138, v94
	s_and_saveexec_b64 s[10:11], vcc
	s_cbranch_execz .LBB0_1780
	v_cmp_gt_f32_e32 vcc, v94, v73
	s_and_saveexec_b64 s[12:13], vcc
	v_mov_b32_e32 v73, v94
	s_or_b64 exec, exec, s[12:13]
	v_mov_b32_e32 v138, v137
	v_mov_b32_e32 v137, v73
.LBB0_1780:
	s_or_b64 exec, exec, s[10:11]
	s_waitcnt lgkmcnt(0)
	v_mov_b32_e32 v79, v180
	v_mov_b32_e32 v74, v154
	s_nop 0
	s_nop 0
	v_mov_b32_e32 v75, v181
	v_mov_b32_e32 v73, v155
	v_max_f32_e32 v68, 0xf149f2ca, v74
	v_cmp_ngt_f32_e32 vcc, v73, v68
	v_mov_b32_e32 v64, v73
	s_and_saveexec_b64 s[10:11], vcc
	s_cbranch_execz .LBB0_1784
	v_mov_b32_e32 v65, 0xf149f2ca
	v_cmp_gt_f32_e32 vcc, v73, v65
	s_and_saveexec_b64 s[12:13], vcc
	v_mov_b32_e32 v65, v73
	s_or_b64 exec, exec, s[12:13]
	v_mov_b32_e32 v64, v68
	v_mov_b32_e32 v68, v65
.LBB0_1784:
	s_or_b64 exec, exec, s[10:11]
	s_nop 0
	s_nop 1
	s_nop 0
	v_mov_b32_e32 v70, v182
	v_mov_b32_e32 v66, v156
	v_cmp_ngt_f32_e32 vcc, v66, v64
	v_mov_b32_e32 v65, v66
	s_and_saveexec_b64 s[10:11], vcc
	s_cbranch_execz .LBB0_1788
	v_cmp_gt_f32_e32 vcc, v66, v68
	s_and_saveexec_b64 s[12:13], vcc
	v_mov_b32_e32 v68, v66
	s_or_b64 exec, exec, s[12:13]
	v_mov_b32_e32 v65, v64
	v_mov_b32_e32 v64, v68
.LBB0_1788:
	s_or_b64 exec, exec, s[10:11]
	s_nop 0
	s_nop 1
	s_nop 0
	v_mov_b32_e32 v71, v183
	v_mov_b32_e32 v67, v157
	v_cmp_ngt_f32_e32 vcc, v67, v65
	v_mov_b32_e32 v68, v67
	s_and_saveexec_b64 s[10:11], vcc
	s_cbranch_execz .LBB0_1792
	v_cmp_gt_f32_e32 vcc, v67, v64
	s_and_saveexec_b64 s[12:13], vcc
	v_mov_b32_e32 v64, v67
	s_or_b64 exec, exec, s[12:13]
	v_mov_b32_e32 v68, v65
	v_mov_b32_e32 v65, v64

.LBB0_5158:
	s_or_b64 exec, exec, s[6:7]
	v_cmp_gt_i32_e64 s[4:5], 16, v167
	v_lshl_add_u32 v188, v167, 2, 0
	s_and_saveexec_b64 s[6:7], s[4:5]
	v_add_u32_e32 v0, 0x20400, v188
	v_mov_b32_e32 v1, 0
	ds_write_b32 v0, v1
	s_or_b64 exec, exec, s[6:7]
	v_readlane_b32 s0, v252, 3
	v_readlane_b32 s1, v252, 4
	s_load_dwordx2 s[0:1], s[0:1], 0xb8
	v_and_b32_e32 v64, 15, v161
	v_ashrrev_i32_e32 v65, 4, v161
	v_lshlrev_b32_e32 v0, 13, v64
	v_lshlrev_b32_e32 v1, 5, v65
	s_waitcnt lgkmcnt(0)
	s_add_u32 s2, s0, s2
	v_readlane_b32 s0, v252, 10
	s_addc_u32 s3, s1, s3
	s_lshl_b32 s0, s0, 10
	s_add_i32 s0, s0, 0
	v_add3_u32 v66, s0, v0, v1
	s_barrier
	ds_read_b128 v[4:7], v66
	ds_read_b128 v[8:11], v66 offset:16
	s_waitcnt lgkmcnt(1)
	v_cvt_pk_bf16_f32 v0, v4, v5
	s_nop 0
	v_lshlrev_b32_e32 v1, 16, v0
	v_and_b32_e32 v2, 0xffff0000, v0
	v_sub_f32_e32 v1, v4, v1
	v_sub_f32_e32 v2, v5, v2
	v_cvt_pk_bf16_f32 v4, v1, v2
	v_cvt_pk_bf16_f32 v1, v6, v7
	s_lshl_b32 s1, s92, 3
	v_lshlrev_b32_e32 v2, 16, v1
	v_and_b32_e32 v3, 0xffff0000, v1
	v_sub_f32_e32 v2, v6, v2
	v_sub_f32_e32 v3, v7, v3
	v_cvt_pk_bf16_f32 v5, v2, v3
	s_waitcnt lgkmcnt(0)
	v_cvt_pk_bf16_f32 v2, v8, v9
	s_lshl_b32 s33, s79, 3
	v_lshlrev_b32_e32 v3, 16, v2
	v_and_b32_e32 v6, 0xffff0000, v2
	v_sub_f32_e32 v3, v8, v3
	v_sub_f32_e32 v6, v9, v6
	v_cvt_pk_bf16_f32 v6, v3, v6
	v_cvt_pk_bf16_f32 v3, v10, v11
	s_mov_b32 s34, 0
	v_lshlrev_b32_e32 v7, 16, v3
	v_sub_f32_e32 v7, v10, v7
	v_and_b32_e32 v8, 0xffff0000, v3
	v_sub_f32_e32 v8, v11, v8
	v_cvt_pk_bf16_f32 v7, v7, v8
	ds_read_b128 v[12:15], v66 offset:128
	ds_read_b128 v[16:19], v66 offset:144
	s_waitcnt lgkmcnt(1)
	v_cvt_pk_bf16_f32 v8, v12, v13
	s_nop 0
	v_lshlrev_b32_e32 v9, 16, v8
	v_and_b32_e32 v10, 0xffff0000, v8
	v_sub_f32_e32 v9, v12, v9
	v_sub_f32_e32 v10, v13, v10
	v_cvt_pk_bf16_f32 v12, v9, v10
	v_cvt_pk_bf16_f32 v9, v14, v15
	v_mov_b32_e32 v189, v161
	v_lshlrev_b32_e32 v10, 16, v9
	v_and_b32_e32 v11, 0xffff0000, v9
	v_sub_f32_e32 v10, v14, v10
	v_sub_f32_e32 v11, v15, v11
	v_cvt_pk_bf16_f32 v13, v10, v11
	s_waitcnt lgkmcnt(0)
	v_cvt_pk_bf16_f32 v10, v16, v17
	s_cmp_lt_i32 s39, 1
	v_lshlrev_b32_e32 v11, 16, v10
	v_and_b32_e32 v14, 0xffff0000, v10
	v_sub_f32_e32 v11, v16, v11
	v_sub_f32_e32 v14, v17, v14
	v_cvt_pk_bf16_f32 v14, v11, v14
	v_cvt_pk_bf16_f32 v11, v18, v19
	s_nop 0
	v_lshlrev_b32_e32 v15, 16, v11
	v_sub_f32_e32 v15, v18, v15
	v_and_b32_e32 v16, 0xffff0000, v11
	v_sub_f32_e32 v16, v19, v16
	v_cvt_pk_bf16_f32 v15, v15, v16
	ds_read_b128 v[20:23], v66 offset:256
	ds_read_b128 v[24:27], v66 offset:272
	s_waitcnt lgkmcnt(1)
	v_cvt_pk_bf16_f32 v16, v20, v21
	s_nop 0
	v_lshlrev_b32_e32 v17, 16, v16
	v_and_b32_e32 v18, 0xffff0000, v16
	v_sub_f32_e32 v17, v20, v17
	v_sub_f32_e32 v18, v21, v18
	v_cvt_pk_bf16_f32 v20, v17, v18
	v_cvt_pk_bf16_f32 v17, v22, v23
	s_nop 0
	v_lshlrev_b32_e32 v18, 16, v17
	v_and_b32_e32 v19, 0xffff0000, v17
	v_sub_f32_e32 v18, v22, v18
	v_sub_f32_e32 v19, v23, v19
	v_cvt_pk_bf16_f32 v21, v18, v19
	s_waitcnt lgkmcnt(0)
	v_cvt_pk_bf16_f32 v18, v24, v25
	s_nop 0
	v_lshlrev_b32_e32 v19, 16, v18
	v_and_b32_e32 v22, 0xffff0000, v18
	v_sub_f32_e32 v19, v24, v19
	v_sub_f32_e32 v22, v25, v22
	v_cvt_pk_bf16_f32 v22, v19, v22
	v_cvt_pk_bf16_f32 v19, v26, v27
	s_nop 0
	v_lshlrev_b32_e32 v23, 16, v19
	v_sub_f32_e32 v23, v26, v23
	v_and_b32_e32 v24, 0xffff0000, v19
	v_sub_f32_e32 v24, v27, v24
	v_cvt_pk_bf16_f32 v23, v23, v24
	ds_read_b128 v[28:31], v66 offset:384
	ds_read_b128 v[32:35], v66 offset:400
	s_waitcnt lgkmcnt(1)
	v_cvt_pk_bf16_f32 v24, v28, v29
	s_nop 0
	v_lshlrev_b32_e32 v25, 16, v24
	v_and_b32_e32 v26, 0xffff0000, v24
	v_sub_f32_e32 v25, v28, v25
	v_sub_f32_e32 v26, v29, v26
	v_cvt_pk_bf16_f32 v28, v25, v26
	v_cvt_pk_bf16_f32 v25, v30, v31
	s_nop 0
	v_lshlrev_b32_e32 v26, 16, v25
	v_and_b32_e32 v27, 0xffff0000, v25
	v_sub_f32_e32 v26, v30, v26
	v_sub_f32_e32 v27, v31, v27
	v_cvt_pk_bf16_f32 v29, v26, v27
	s_waitcnt lgkmcnt(0)
	v_cvt_pk_bf16_f32 v26, v32, v33
	s_nop 0
	v_lshlrev_b32_e32 v27, 16, v26
	v_and_b32_e32 v30, 0xffff0000, v26
	v_sub_f32_e32 v27, v32, v27
	v_sub_f32_e32 v30, v33, v30
	v_cvt_pk_bf16_f32 v30, v27, v30
	v_cvt_pk_bf16_f32 v27, v34, v35
	s_nop 0
	v_lshlrev_b32_e32 v31, 16, v27
	v_sub_f32_e32 v31, v34, v31
	v_and_b32_e32 v32, 0xffff0000, v27
	v_sub_f32_e32 v32, v35, v32
	v_cvt_pk_bf16_f32 v31, v31, v32
	s_waitcnt vmcnt(7)
	ds_read_b128 v[36:39], v66 offset:512
	ds_read_b128 v[40:43], v66 offset:528
	s_waitcnt lgkmcnt(1)
	v_cvt_pk_bf16_f32 v32, v36, v37
	s_nop 0
	v_lshlrev_b32_e32 v33, 16, v32
	v_and_b32_e32 v34, 0xffff0000, v32
	v_sub_f32_e32 v33, v36, v33
	v_sub_f32_e32 v34, v37, v34
	v_cvt_pk_bf16_f32 v36, v33, v34
	v_cvt_pk_bf16_f32 v33, v38, v39
	s_nop 0
	v_lshlrev_b32_e32 v34, 16, v33
	v_and_b32_e32 v35, 0xffff0000, v33
	v_sub_f32_e32 v34, v38, v34
	v_sub_f32_e32 v35, v39, v35
	v_cvt_pk_bf16_f32 v37, v34, v35
	s_waitcnt lgkmcnt(0)
	v_cvt_pk_bf16_f32 v34, v40, v41
	s_nop 0
	v_lshlrev_b32_e32 v35, 16, v34
	v_and_b32_e32 v38, 0xffff0000, v34
	v_sub_f32_e32 v35, v40, v35
	v_sub_f32_e32 v38, v41, v38
	v_cvt_pk_bf16_f32 v38, v35, v38
	v_cvt_pk_bf16_f32 v35, v42, v43
	s_nop 0
	v_lshlrev_b32_e32 v39, 16, v35
	v_sub_f32_e32 v39, v42, v39
	v_and_b32_e32 v40, 0xffff0000, v35
	v_sub_f32_e32 v40, v43, v40
	v_cvt_pk_bf16_f32 v39, v39, v40
	s_waitcnt vmcnt(1)
	ds_read_b128 v[44:47], v66 offset:640
	s_waitcnt vmcnt(0)
	ds_read_b128 v[48:51], v66 offset:656
	s_waitcnt lgkmcnt(1)
	v_cvt_pk_bf16_f32 v40, v44, v45
	s_nop 0
	v_lshlrev_b32_e32 v41, 16, v40
	v_and_b32_e32 v42, 0xffff0000, v40
	v_sub_f32_e32 v41, v44, v41
	v_sub_f32_e32 v42, v45, v42
	v_cvt_pk_bf16_f32 v44, v41, v42
	v_cvt_pk_bf16_f32 v41, v46, v47
	s_nop 0
	v_lshlrev_b32_e32 v42, 16, v41
	v_and_b32_e32 v43, 0xffff0000, v41
	v_sub_f32_e32 v42, v46, v42
	v_sub_f32_e32 v43, v47, v43
	v_cvt_pk_bf16_f32 v45, v42, v43
	s_waitcnt lgkmcnt(0)
	v_cvt_pk_bf16_f32 v42, v48, v49
	s_nop 0
	v_lshlrev_b32_e32 v43, 16, v42
	v_and_b32_e32 v46, 0xffff0000, v42
	v_sub_f32_e32 v43, v48, v43
	v_sub_f32_e32 v46, v49, v46
	v_cvt_pk_bf16_f32 v46, v43, v46
	v_cvt_pk_bf16_f32 v43, v50, v51
	s_nop 0
	v_lshlrev_b32_e32 v47, 16, v43
	v_sub_f32_e32 v47, v50, v47
	v_and_b32_e32 v48, 0xffff0000, v43
	v_sub_f32_e32 v48, v51, v48
	v_cvt_pk_bf16_f32 v47, v47, v48
	ds_read_b128 v[52:55], v66 offset:768
	ds_read_b128 v[56:59], v66 offset:784
	s_waitcnt lgkmcnt(1)
	v_cvt_pk_bf16_f32 v48, v52, v53
	s_nop 0
	v_lshlrev_b32_e32 v49, 16, v48
	v_and_b32_e32 v50, 0xffff0000, v48
	v_sub_f32_e32 v49, v52, v49
	v_sub_f32_e32 v50, v53, v50
	v_cvt_pk_bf16_f32 v52, v49, v50
	v_cvt_pk_bf16_f32 v49, v54, v55
	s_nop 0
	v_lshlrev_b32_e32 v50, 16, v49
	v_and_b32_e32 v51, 0xffff0000, v49
	v_sub_f32_e32 v50, v54, v50
	v_sub_f32_e32 v51, v55, v51
	v_cvt_pk_bf16_f32 v53, v50, v51
	s_waitcnt lgkmcnt(0)
	v_cvt_pk_bf16_f32 v50, v56, v57
	s_nop 0
	v_lshlrev_b32_e32 v51, 16, v50
	v_and_b32_e32 v54, 0xffff0000, v50
	v_sub_f32_e32 v51, v56, v51
	v_sub_f32_e32 v54, v57, v54
	v_cvt_pk_bf16_f32 v54, v51, v54
	v_cvt_pk_bf16_f32 v51, v58, v59
	s_nop 0
	v_lshlrev_b32_e32 v55, 16, v51
	v_sub_f32_e32 v55, v58, v55
	v_and_b32_e32 v56, 0xffff0000, v51
	v_sub_f32_e32 v56, v59, v56
	v_cvt_pk_bf16_f32 v55, v55, v56
	ds_read_b128 v[60:63], v66 offset:896
	ds_read_b128 v[66:69], v66 offset:912
	s_waitcnt lgkmcnt(1)
	v_cvt_pk_bf16_f32 v56, v60, v61
	s_nop 0
	v_lshlrev_b32_e32 v57, 16, v56
	v_and_b32_e32 v58, 0xffff0000, v56
	v_sub_f32_e32 v57, v60, v57
	v_sub_f32_e32 v58, v61, v58
	v_cvt_pk_bf16_f32 v60, v57, v58
	v_cvt_pk_bf16_f32 v57, v62, v63
	s_nop 0
	v_lshlrev_b32_e32 v58, 16, v57
	v_and_b32_e32 v59, 0xffff0000, v57
	v_sub_f32_e32 v58, v62, v58
	v_sub_f32_e32 v59, v63, v59
	v_cvt_pk_bf16_f32 v61, v58, v59
	s_waitcnt lgkmcnt(0)
	v_cvt_pk_bf16_f32 v58, v66, v67
	s_nop 0
	v_lshlrev_b32_e32 v59, 16, v58
	v_and_b32_e32 v62, 0xffff0000, v58
	v_sub_f32_e32 v59, v66, v59
	v_sub_f32_e32 v62, v67, v62
	v_cvt_pk_bf16_f32 v62, v59, v62
	v_cvt_pk_bf16_f32 v59, v68, v69
	s_nop 0
	v_lshlrev_b32_e32 v63, 16, v59
	v_sub_f32_e32 v63, v68, v63
	v_and_b32_e32 v66, 0xffff0000, v59
	v_sub_f32_e32 v66, v69, v66
	v_cvt_pk_bf16_f32 v63, v63, v66
	s_barrier
	s_cbranch_scc1 .LBB0_5287
	v_readlane_b32 s8, v252, 3
	s_add_u32 s35, s2, 0x1c9c8000
	v_readlane_b32 s9, v252, 4
	s_addc_u32 s36, s3, 0
	s_load_dwordx2 s[6:7], s[8:9], 0x28
	s_load_dwordx2 s[20:21], s[8:9], 0x88
	s_add_u32 s37, s2, 0x149c8000
	v_readlane_b32 s10, v252, 10
	s_addc_u32 s40, s3, 0
	s_add_i32 s18, s10, s33
	s_add_u32 s41, s2, 0x249c8000
	s_addc_u32 s42, s3, 0
	s_waitcnt lgkmcnt(0)
	s_add_u32 s22, s6, 0x2000
	s_addc_u32 s23, s7, 0
	s_add_i32 s6, s18, s1
	s_ashr_i32 s7, s6, 31
	s_lshl_b64 s[8:9], s[6:7], 11
	s_add_u32 s8, s37, s8
	s_addc_u32 s9, s40, s9
	v_lshlrev_b32_e32 v66, 2, v189
	s_lshl_b64 s[6:7], s[6:7], 12
	v_ashrrev_i32_e32 v67, 31, v66
	s_add_u32 s6, s35, s6
	s_addc_u32 s7, s36, s7
	v_lshlrev_b64 v[70:71], 1, v[66:67]
	s_ashr_i32 s19, s18, 31
	v_lshl_add_u64 v[72:73], s[6:7], 0, v[70:71]
	s_lshl_b64 s[6:7], s[18:19], 11
	s_add_u32 s6, s37, s6
	s_addc_u32 s7, s40, s7
	v_lshl_add_u64 v[68:69], s[8:9], 0, v[66:67]
	v_lshl_add_u64 v[66:67], s[6:7], 0, v[66:67]
	s_lshl_b64 s[6:7], s[18:19], 12
	s_add_u32 s6, s35, s6
	s_addc_u32 s7, s36, s7
	global_load_dwordx2 v[142:143], v[72:73], off offset:3584
	global_load_dwordx2 v[132:133], v[72:73], off offset:3072
	global_load_dwordx2 v[90:91], v[72:73], off offset:2560
	global_load_dwordx2 v[88:89], v[72:73], off offset:2048
	global_load_dword v154, v[68:69], off offset:1792
	global_load_dword v155, v[68:69], off offset:1536
	global_load_dword v160, v[68:69], off offset:1280
	global_load_dword v166, v[68:69], off offset:1024
	global_load_dword v168, v[68:69], off offset:768
	global_load_dword v169, v[68:69], off offset:512
	global_load_dword v172, v[68:69], off offset:256
	global_load_dword v170, v[68:69], off
	global_load_dwordx2 v[136:137], v[72:73], off offset:1536
	global_load_dwordx2 v[128:129], v[72:73], off offset:1024
	global_load_dwordx2 v[138:139], v[72:73], off offset:512
	global_load_dwordx2 v[140:141], v[72:73], off
	v_lshl_add_u64 v[68:69], s[6:7], 0, v[70:71]
	global_load_dwordx2 v[144:145], v[68:69], off offset:3584
	global_load_dwordx2 v[86:87], v[68:69], off offset:3072
	global_load_dwordx2 v[82:83], v[68:69], off offset:2560
	global_load_dwordx2 v[80:81], v[68:69], off offset:2048
	global_load_dword v171, v[66:67], off offset:1792
	global_load_dword v173, v[66:67], off offset:1536
	global_load_dword v134, v[66:67], off offset:1280
	global_load_dword v135, v[66:67], off offset:1024
	global_load_dword v148, v[66:67], off offset:768
	global_load_dword v149, v[66:67], off offset:512
	global_load_dword v150, v[66:67], off offset:256
	global_load_dword v146, v[66:67], off
	global_load_dwordx2 v[92:93], v[68:69], off offset:1536
	global_load_dwordx2 v[84:85], v[68:69], off offset:1024
	global_load_dwordx2 v[94:95], v[68:69], off offset:512
	global_load_dwordx2 v[130:131], v[68:69], off
	v_lshl_add_u32 v65, s10, 5, v65
	v_lshl_add_u32 v66, v64, 12, 0
	v_xor_b32_e32 v69, v65, v64
	v_lshl_add_u32 v190, v69, 4, v66
	v_add_u32_e32 v69, 4, v65
	v_xor_b32_e32 v69, v69, v64
	v_lshl_add_u32 v192, v69, 4, v66
	v_add_u32_e32 v69, 8, v65
	v_xor_b32_e32 v69, v69, v64
	v_lshl_add_u32 v194, v69, 4, v66
	v_add_u32_e32 v69, 12, v65
	v_xor_b32_e32 v69, v69, v64
	v_lshl_add_u32 v196, v69, 4, v66
	v_add_u32_e32 v69, 16, v65
	s_lshl_b32 s43, s10, 1
	s_add_i32 s6, s0, 0x22000
	v_xor_b32_e32 v69, v69, v64
	s_add_u32 s24, s2, 0x468000
	v_lshl_add_u32 v198, v69, 4, v66
	v_add_u32_e32 v69, 20, v65
	s_addc_u32 s25, s3, 0
	v_xor_b32_e32 v69, v69, v64
	s_add_u32 s26, s2, 0x488000
	v_lshl_add_u32 v200, v69, 4, v66
	v_add_u32_e32 v69, 24, v65
	v_add_u32_e32 v65, 28, v65
	v_lshl_add_u32 v67, v64, 6, s6
	s_addc_u32 s27, s3, 0
	s_lshl_b32 s6, s10, 13
	s_or_b32 s45, s43, 1
	v_xor_b32_e32 v69, v69, v64
	v_xor_b32_e32 v64, v65, v64
	v_and_b32_e32 v68, -16, v161
	s_add_i32 s44, s6, 0
	s_lshl_b32 s6, s45, 12
	v_lshl_add_u32 v202, v69, 4, v66
	v_lshl_add_u32 v204, v64, 4, v66
	s_add_i32 s46, s6, 0
	v_add_u32_e32 v191, 0x10000, v190
	v_add_u32_e32 v193, 0x10000, v192
	v_add_u32_e32 v195, 0x10000, v194
	v_add_u32_e32 v197, 0x10000, v196
	v_add_u32_e32 v199, 0x10000, v198
	v_add_u32_e32 v201, 0x10000, v200
	v_add_u32_e32 v203, 0x10000, v202
	v_add_u32_e32 v205, 0x10000, v204
	s_mul_i32 s47, s92, 24
	s_movk_i32 s48, 0x100
	v_mov_b32_e32 v206, 0x358637bd
	s_mov_b32 s49, 0xf800000
	v_mov_b32_e32 v207, 0x260
	v_add_u32_e32 v208, v67, v68
	v_mov_b32_e32 v209, 0
	s_mov_b32 s50, 0xbfb8aa3b
	s_mov_b32 s51, 0x42ce8ed0
	s_mov_b32 s52, 0xc2b17218
	s_mov_b32 s53, 0xf149f2ca
	v_mov_b32_e32 v210, 1
	s_add_i32 s54, 0, 0x20400
	s_add_i32 s55, 0, 0x20500
	v_mov_b32_e32 v211, 0x7f800000
	s_mov_b32 s56, 0
	s_waitcnt lgkmcnt(0)
	v_and_b32_e32 v249, 15, v167
	v_lshlrev_b32_e32 v249, 2, v249
	global_load_dword v249, v249, s[20:21]
	s_branch .LBB0_5166

.Lpf_skip_1:
	v_lshlrev_b32_e32 v90, 16, v88
	v_and_b32_e32 v91, 0xffff0000, v88
	v_sub_f32_e32 v90, v86, v90
	v_sub_f32_e32 v91, v87, v91
	v_cvt_pk_bf16_f32 v89, v84, v85
	v_cvt_pk_bf16_f32 v90, v90, v91
	v_lshlrev_b32_e32 v128, 4, v128
	v_lshlrev_b32_e32 v91, 16, v89
	v_sub_f32_e32 v91, v84, v91
	v_and_b32_e32 v129, 0xffff0000, v89
	v_add3_u32 v128, s46, v128, v228
	v_sub_f32_e32 v129, v85, v129
	v_cvt_pk_bf16_f32 v91, v91, v129
	ds_write_b64 v128, v[88:89]
	v_add_u32_e32 v88, 0x10000, v128
	ds_write_b64 v88, v[90:91]
	v_mov_b32_e32 v90, 0
	v_cvt_pk_fp8_f32 v90, v154, v155
	v_mov_b32_e32 v91, 0
	v_cvt_pk_fp8_f32 v91, v174, v175
	v_lshl_add_u64 v[88:89], s[6:7], 0, v[78:79]
	v_cvt_pk_fp8_f32 v90, v152, v153 op_sel:[0,0,1]
	v_mov_b32_e32 v128, 0
	v_cvt_pk_fp8_f32 v91, v170, v171 op_sel:[0,0,1]
	v_cvt_pk_fp8_f32 v128, v186, v187
	global_store_dword v[88:89], v90, off
	v_lshl_add_u64 v[88:89], s[6:7], 0, v[76:77]
	v_mov_b32_e32 v90, 0
	global_store_dword v[88:89], v91, off
	v_cvt_pk_fp8_f32 v90, v158, v159
	v_mov_b32_e32 v91, 0
	v_cvt_pk_fp8_f32 v91, v178, v179
	v_cvt_pk_fp8_f32 v128, v184, v185 op_sel:[0,0,1]
	v_cvt_pk_fp8_f32 v90, v156, v157 op_sel:[0,0,1]
	v_lshl_add_u64 v[88:89], s[6:7], 0, v[74:75]
	v_cvt_pk_fp8_f32 v91, v176, v177 op_sel:[0,0,1]
	global_store_dword v[88:89], v128, off
	v_lshl_add_u64 v[88:89], s[6:7], 0, v[72:73]
	v_mov_b32_e32 v128, 0
	global_store_dword v[88:89], v90, off
	v_lshl_add_u64 v[88:89], s[6:7], 0, v[70:71]
	v_cvt_pk_fp8_f32 v128, v134, v135
	global_store_dword v[88:89], v91, off
	v_mov_b32_e32 v88, 0
	v_cvt_pk_fp8_f32 v88, v144, v145
	v_mov_b32_e32 v89, 0
	v_cvt_pk_fp8_f32 v89, v80, v81
	v_cvt_pk_fp8_f32 v128, v130, v131 op_sel:[0,0,1]
	v_cvt_pk_fp8_f32 v88, v242, v243 op_sel:[0,0,1]
	v_lshl_add_u64 v[80:81], s[6:7], 0, v[68:69]
	v_cvt_pk_fp8_f32 v89, v82, v83 op_sel:[0,0,1]
	global_store_dword v[80:81], v128, off
	v_lshl_add_u64 v[80:81], s[6:7], 0, v[66:67]
	global_store_dword v[80:81], v88, off
	v_lshl_add_u64 v[80:81], s[6:7], 0, v[64:65]
	global_store_dword v[80:81], v89, off
	v_mov_b32_e32 v80, 0
	v_mov_b32_e32 v81, 0
	v_cvt_pk_fp8_f32 v80, v146, v147
	v_cvt_pk_fp8_f32 v81, v164, v165
	s_add_i32 s6, s1, s18
	s_ashr_i32 s7, s6, 31
	s_lshl_b64 s[6:7], s[6:7], 11
	v_cvt_pk_fp8_f32 v80, v142, v143 op_sel:[0,0,1]
	v_cvt_pk_fp8_f32 v81, v162, v163 op_sel:[0,0,1]
	s_add_u32 s6, s41, s6
	s_addc_u32 s7, s42, s7
	v_lshl_add_u64 v[78:79], s[6:7], 0, v[78:79]
	v_lshl_add_u64 v[76:77], s[6:7], 0, v[76:77]
	v_mov_b32_e32 v82, 0
	global_store_dword v[78:79], v80, off
	global_store_dword v[76:77], v81, off
	v_mov_b32_e32 v76, 0
	v_mov_b32_e32 v77, 0
	v_cvt_pk_fp8_f32 v82, v182, v183
	v_cvt_pk_fp8_f32 v76, v150, v151
	v_cvt_pk_fp8_f32 v77, v172, v173
	v_lshl_add_u64 v[74:75], s[6:7], 0, v[74:75]
	v_cvt_pk_fp8_f32 v82, v180, v181 op_sel:[0,0,1]
	v_cvt_pk_fp8_f32 v76, v148, v149 op_sel:[0,0,1]
	v_cvt_pk_fp8_f32 v77, v168, v169 op_sel:[0,0,1]
	v_lshl_add_u64 v[72:73], s[6:7], 0, v[72:73]
	v_lshl_add_u64 v[70:71], s[6:7], 0, v[70:71]
	global_store_dword v[74:75], v82, off
	v_mov_b32_e32 v74, 0
	global_store_dword v[72:73], v76, off
	global_store_dword v[70:71], v77, off
	v_mov_b32_e32 v70, 0
	v_mov_b32_e32 v71, 0
	v_cvt_pk_fp8_f32 v74, v94, v95
	v_cvt_pk_fp8_f32 v70, v138, v139
	v_cvt_pk_fp8_f32 v71, v86, v87
	v_lshl_add_u64 v[68:69], s[6:7], 0, v[68:69]
	v_cvt_pk_fp8_f32 v74, v92, v93 op_sel:[0,0,1]
	v_cvt_pk_fp8_f32 v70, v136, v137 op_sel:[0,0,1]
	v_cvt_pk_fp8_f32 v71, v84, v85 op_sel:[0,0,1]
	v_lshl_add_u64 v[66:67], s[6:7], 0, v[66:67]
	v_lshl_add_u64 v[64:65], s[6:7], 0, v[64:65]
	global_store_dword v[68:69], v74, off
	global_store_dword v[66:67], v70, off
	global_store_dword v[64:65], v71, off
	s_waitcnt lgkmcnt(0)
	s_barrier
	ds_read_b128 v[64:67], v190
	ds_read_b128 v[68:71], v191
	s_waitcnt lgkmcnt(1)
	v_mfma_f32_16x16x32_bf16 v[72:75], v[0:3], v[64:67], 0
	v_mov_b32_e32 v128, v167
	v_mfma_f32_16x16x32_bf16 v[64:67], v[4:7], v[64:67], v[72:75]
	s_waitcnt lgkmcnt(0)
	v_mfma_f32_16x16x32_bf16 v[64:67], v[0:3], v[68:71], v[64:67]
	ds_read_b128 v[68:71], v192
	s_nop 2
	ds_read_b128 v[72:75], v193
	s_waitcnt lgkmcnt(1)
	v_mfma_f32_16x16x32_bf16 v[64:67], v[8:11], v[68:71], v[64:67]
	v_mfma_f32_16x16x32_bf16 v[64:67], v[12:15], v[68:71], v[64:67]
	s_waitcnt lgkmcnt(0)
	v_mfma_f32_16x16x32_bf16 v[64:67], v[8:11], v[72:75], v[64:67]
	ds_read_b128 v[68:71], v194
	ds_read_b128 v[72:75], v195
	s_waitcnt lgkmcnt(1)
	v_mfma_f32_16x16x32_bf16 v[64:67], v[16:19], v[68:71], v[64:67]
	v_mfma_f32_16x16x32_bf16 v[64:67], v[20:23], v[68:71], v[64:67]
	s_waitcnt lgkmcnt(0)
	v_mfma_f32_16x16x32_bf16 v[64:67], v[16:19], v[72:75], v[64:67]
	ds_read_b128 v[68:71], v196
	ds_read_b128 v[72:75], v197
	s_waitcnt lgkmcnt(1)
	v_mfma_f32_16x16x32_bf16 v[64:67], v[24:27], v[68:71], v[64:67]
	v_mfma_f32_16x16x32_bf16 v[64:67], v[28:31], v[68:71], v[64:67]
	s_waitcnt lgkmcnt(0)
	v_mfma_f32_16x16x32_bf16 v[64:67], v[24:27], v[72:75], v[64:67]
	ds_read_b128 v[68:71], v198
	ds_read_b128 v[72:75], v199
	s_waitcnt lgkmcnt(1)
	v_mfma_f32_16x16x32_bf16 v[64:67], v[32:35], v[68:71], v[64:67]
	v_mfma_f32_16x16x32_bf16 v[64:67], v[36:39], v[68:71], v[64:67]
	s_waitcnt lgkmcnt(0)
	v_mfma_f32_16x16x32_bf16 v[64:67], v[32:35], v[72:75], v[64:67]
	ds_read_b128 v[68:71], v200
	ds_read_b128 v[72:75], v201
	s_waitcnt lgkmcnt(1)
	v_mfma_f32_16x16x32_bf16 v[64:67], v[40:43], v[68:71], v[64:67]
	v_mfma_f32_16x16x32_bf16 v[64:67], v[44:47], v[68:71], v[64:67]
	s_waitcnt lgkmcnt(0)
	v_mfma_f32_16x16x32_bf16 v[64:67], v[40:43], v[72:75], v[64:67]
	ds_read_b128 v[68:71], v202
	ds_read_b128 v[72:75], v203
	s_waitcnt lgkmcnt(1)
	v_mfma_f32_16x16x32_bf16 v[64:67], v[48:51], v[68:71], v[64:67]
	v_mfma_f32_16x16x32_bf16 v[64:67], v[52:55], v[68:71], v[64:67]
	s_waitcnt lgkmcnt(0)
	v_mfma_f32_16x16x32_bf16 v[64:67], v[48:51], v[72:75], v[64:67]
	ds_read_b128 v[68:71], v204
	ds_read_b128 v[72:75], v205
	s_waitcnt lgkmcnt(1)
	v_mfma_f32_16x16x32_bf16 v[64:67], v[56:59], v[68:71], v[64:67]
	v_mfma_f32_16x16x32_bf16 v[64:67], v[60:63], v[68:71], v[64:67]
	s_waitcnt lgkmcnt(0)
	v_mfma_f32_16x16x32_bf16 v[64:67], v[56:59], v[72:75], v[64:67]
	s_nop 7
	ds_write_b128 v208, v[64:67]
	s_waitcnt lgkmcnt(0)
	s_barrier
	s_nop 0
	v_cmp_gt_i32_e32 vcc, s48, v128
	s_and_saveexec_b64 s[6:7], vcc
	s_cbranch_execz .LBB0_5172
	v_lshl_add_u32 v72, v128, 2, 0
	v_add_u32_e32 v70, 0x22000, v72
	ds_read2st64_b32 v[64:65], v70 offset1:4
	ds_read2st64_b32 v[66:67], v70 offset0:8 offset1:12
	ds_read2st64_b32 v[68:69], v70 offset0:16 offset1:20
	ds_read2st64_b32 v[70:71], v70 offset0:24 offset1:28
	s_waitcnt lgkmcnt(3)
	v_add_f32_e32 v64, 0, v64
	v_add_f32_e32 v64, v64, v65
	s_waitcnt lgkmcnt(2)
	v_add_f32_e32 v64, v64, v66
	v_add_f32_e32 v64, v64, v67
	s_waitcnt lgkmcnt(1)
	v_add_f32_e32 v64, v64, v68
	v_add_f32_e32 v64, v64, v69
	s_waitcnt lgkmcnt(0)
	v_add_f32_e32 v64, v64, v70
	v_add_f32_e32 v64, v64, v71
	v_add_u32_e32 v65, 0x21000, v72
	ds_write_b32 v65, v64
	v_mul_f32_e32 v142, 0xbfb8aa3b, v64
	v_fma_f32 v143, v64, s50, -v142
	v_rndne_f32_e32 v144, v142
	v_fmac_f32_e32 v143, 0xb2a5705f, v64
	v_sub_f32_e32 v142, v142, v144
	v_add_f32_e32 v142, v142, v143
	v_cvt_i32_f32_e32 v145, v144
	v_exp_f32_e32 v146, v142
	v_cmp_nlt_f32_e32 vcc, s51, v64
	v_ldexp_f32 v145, v146, v145
	s_nop 0
	v_cndmask_b32_e32 v145, 0, v145, vcc
	v_cmp_ngt_f32_e32 vcc, s52, v64
	s_nop 1
	v_cndmask_b32_e32 v145, v211, v145, vcc
	v_add_f32_e32 v145, 1.0, v145
	v_div_scale_f32 v146, s[98:99], v145, v145, 1.0
	v_rcp_f32_e32 v147, v146
	v_div_scale_f32 v148, vcc, 1.0, v145, 1.0
	v_fma_f32 v149, -v146, v147, 1.0
	v_fmac_f32_e32 v147, v149, v147
	v_mul_f32_e32 v149, v148, v147
	v_fma_f32 v150, -v146, v149, v148
	v_fmac_f32_e32 v149, v150, v147
	v_fma_f32 v146, -v146, v149, v148
	v_div_fmas_f32 v146, v146, v147, v149
	v_div_fixup_f32 v146, v146, v145, 1.0
	ds_write_b32 v65, v146 offset:1024
	v_add_f32_e32 v147, v249, v146
	ds_write_b32 v65, v147 offset:2048
